# mLSTM pass-2 item prologue: N0 and stabiliser loads share the gate fetch's single wait (their LDS writes deferred behind it) - three serial round trips become one
# baseline (speedup 1.0000x reference)
; template <bool PASS2, int DIRT>
; DI void mlstm_item(const Params& P, LAS unsigned char* lds, int st, int g) {
;     ...
;     __syncthreads();
;     if (PASS2) {
;         const float* ec = (const float*)(P.ws + WS_ENTC) + ((size_t)st * 16 + g) * 32768;
; #pragma unroll
;         for (int dkt = 0; dkt < 4; ++dkt)
; #pragma unroll
;             for (int e = 0; e < 16; ++e) C[dkt][e] = ec[(32 * dkt + (e & 3) + 8 * (e >> 2) + 4 * hh) * 256 + 32 * wid + r];
.LBB0_709:
	s_getreg_b32 s0, hwreg(HW_REG_HW_ID, 0, 6)
	s_and_b32 s0, s0, 63
	s_lshl_b32 s0, s0, 2
	s_add_i32 s0, s0, 0
	s_add_i32 s0, s0, 0x24400
	v_mov_b32_e32 v0, s0
	ds_read_b32 v195, v0
	s_and_b32 s96, s42, 15
	s_cmpk_lt_u32 s42, 0x80
	s_mov_b64 s[2:3], -1
	s_cbranch_scc1 .LBB0_766
	s_ashr_i32 s4, s42, 4
	s_ashr_i32 s5, s4, 31
	s_lshl_b64 s[6:7], s[4:5], 4
	s_waitcnt lgkmcnt(0)
	v_readfirstlane_b32 s1, v195
	s_or_b32 s6, s6, s96
	s_lshl_b32 s97, s1, 6
	s_lshl_b64 s[2:3], s[6:7], 17
	s_add_u32 s8, s53, s2
	s_waitcnt vmcnt(2)
	v_mbcnt_lo_u32_b32 v70, -1, 0
	v_mbcnt_hi_u32_b32 v70, -1, v70
	s_addc_u32 s9, s54, s3
	v_lshlrev_b32_e32 v0, 5, v70
	s_lshl_b32 s44, s1, 5
	v_and_b32_e32 v0, 0x400, v0
	v_and_or_b32 v1, v70, 31, s44
	v_add_u32_e32 v56, v0, v1
	v_add_u32_e32 v0, 0x800, v56
	v_ashrrev_i32_e32 v1, 31, v0
	v_lshl_add_u64 v[6:7], v[0:1], 2, s[8:9]
	v_add_u32_e32 v0, 0x900, v56
	v_ashrrev_i32_e32 v1, 31, v0
	v_lshl_add_u64 v[8:9], v[0:1], 2, s[8:9]
	v_add_u32_e32 v0, 0xa00, v56
	v_ashrrev_i32_e32 v1, 31, v0
	v_lshl_add_u64 v[10:11], v[0:1], 2, s[8:9]
	v_add_u32_e32 v0, 0xb00, v56
	v_ashrrev_i32_e32 v57, 31, v56
	v_ashrrev_i32_e32 v1, 31, v0
	v_lshl_add_u64 v[4:5], v[56:57], 2, s[8:9]
	v_lshl_add_u64 v[12:13], v[0:1], 2, s[8:9]
	s_waitcnt vmcnt(0)
	s_barrier
	global_load_dword v0, v[4:5], off
	global_load_dword v1, v[4:5], off offset:1024
	global_load_dword v2, v[4:5], off offset:2048
	global_load_dword v3, v[4:5], off offset:3072
	s_nop 0
	global_load_dword v4, v[6:7], off
	global_load_dword v5, v[8:9], off
	s_nop 0
	global_load_dword v6, v[10:11], off
	global_load_dword v7, v[12:13], off
	v_add_u32_e32 v8, 0x1000, v56
	v_add_u32_e32 v10, 0x1100, v56
	v_add_u32_e32 v12, 0x1200, v56
	v_add_u32_e32 v14, 0x1300, v56
	v_add_u32_e32 v16, 0x1800, v56
	v_add_u32_e32 v18, 0x1900, v56
	v_add_u32_e32 v20, 0x1a00, v56
	v_add_u32_e32 v22, 0x1b00, v56
	v_ashrrev_i32_e32 v9, 31, v8
	v_ashrrev_i32_e32 v11, 31, v10
	v_ashrrev_i32_e32 v13, 31, v12
	v_ashrrev_i32_e32 v15, 31, v14
	v_ashrrev_i32_e32 v17, 31, v16
	v_ashrrev_i32_e32 v19, 31, v18
	v_ashrrev_i32_e32 v21, 31, v20
	v_ashrrev_i32_e32 v23, 31, v22
	v_lshl_add_u64 v[8:9], v[8:9], 2, s[8:9]
	v_lshl_add_u64 v[10:11], v[10:11], 2, s[8:9]
	v_lshl_add_u64 v[12:13], v[12:13], 2, s[8:9]
	v_lshl_add_u64 v[14:15], v[14:15], 2, s[8:9]
	v_lshl_add_u64 v[16:17], v[16:17], 2, s[8:9]
	v_lshl_add_u64 v[18:19], v[18:19], 2, s[8:9]
	v_lshl_add_u64 v[20:21], v[20:21], 2, s[8:9]
	v_lshl_add_u64 v[22:23], v[22:23], 2, s[8:9]
	global_load_dword v8, v[8:9], off
	s_nop 0
	global_load_dword v9, v[10:11], off
	s_nop 0
	global_load_dword v10, v[12:13], off
	global_load_dword v11, v[14:15], off
	s_nop 0
	global_load_dword v12, v[16:17], off
	global_load_dword v13, v[18:19], off
	global_load_dword v14, v[20:21], off
	global_load_dword v15, v[22:23], off
	v_add_u32_e32 v16, 0x2000, v56
	v_add_u32_e32 v18, 0x2100, v56
	v_add_u32_e32 v20, 0x2200, v56
	v_add_u32_e32 v22, 0x2300, v56
	v_add_u32_e32 v24, 0x2800, v56
	v_add_u32_e32 v26, 0x2900, v56
	v_add_u32_e32 v28, 0x2a00, v56
	v_add_u32_e32 v30, 0x2b00, v56
	v_ashrrev_i32_e32 v17, 31, v16
	v_ashrrev_i32_e32 v19, 31, v18
	v_ashrrev_i32_e32 v21, 31, v20
	v_ashrrev_i32_e32 v23, 31, v22
	v_ashrrev_i32_e32 v25, 31, v24
	v_ashrrev_i32_e32 v27, 31, v26
	v_ashrrev_i32_e32 v29, 31, v28
	v_ashrrev_i32_e32 v31, 31, v30
	v_lshl_add_u64 v[16:17], v[16:17], 2, s[8:9]
	v_lshl_add_u64 v[18:19], v[18:19], 2, s[8:9]
	v_lshl_add_u64 v[20:21], v[20:21], 2, s[8:9]
	v_lshl_add_u64 v[22:23], v[22:23], 2, s[8:9]
	v_lshl_add_u64 v[24:25], v[24:25], 2, s[8:9]
	v_lshl_add_u64 v[26:27], v[26:27], 2, s[8:9]
	v_lshl_add_u64 v[28:29], v[28:29], 2, s[8:9]
	v_lshl_add_u64 v[30:31], v[30:31], 2, s[8:9]
	global_load_dword v16, v[16:17], off
	s_nop 0
	global_load_dword v17, v[18:19], off
	s_nop 0
	global_load_dword v18, v[20:21], off
	global_load_dword v19, v[22:23], off
	s_nop 0
	global_load_dword v20, v[24:25], off
	global_load_dword v21, v[26:27], off
	global_load_dword v22, v[28:29], off
	global_load_dword v23, v[30:31], off
	v_add_u32_e32 v24, 0x3000, v56
	v_add_u32_e32 v26, 0x3100, v56
	v_add_u32_e32 v28, 0x3200, v56
	v_add_u32_e32 v30, 0x3300, v56
	v_add_u32_e32 v32, 0x3800, v56
	v_add_u32_e32 v34, 0x3900, v56
	v_add_u32_e32 v36, 0x3a00, v56
	v_add_u32_e32 v38, 0x3b00, v56
	v_ashrrev_i32_e32 v25, 31, v24
	v_ashrrev_i32_e32 v27, 31, v26
	v_ashrrev_i32_e32 v29, 31, v28
	v_ashrrev_i32_e32 v31, 31, v30
	v_ashrrev_i32_e32 v33, 31, v32
	v_ashrrev_i32_e32 v35, 31, v34
	v_ashrrev_i32_e32 v37, 31, v36
	v_ashrrev_i32_e32 v39, 31, v38
	v_lshl_add_u64 v[24:25], v[24:25], 2, s[8:9]
	v_lshl_add_u64 v[26:27], v[26:27], 2, s[8:9]
	v_lshl_add_u64 v[28:29], v[28:29], 2, s[8:9]
	v_lshl_add_u64 v[30:31], v[30:31], 2, s[8:9]
	v_lshl_add_u64 v[32:33], v[32:33], 2, s[8:9]
	v_lshl_add_u64 v[34:35], v[34:35], 2, s[8:9]
	v_lshl_add_u64 v[36:37], v[36:37], 2, s[8:9]
	v_lshl_add_u64 v[38:39], v[38:39], 2, s[8:9]
	global_load_dword v24, v[24:25], off
	s_nop 0
	global_load_dword v25, v[26:27], off
	s_nop 0
	global_load_dword v26, v[28:29], off
	global_load_dword v27, v[30:31], off
	s_nop 0
	global_load_dword v28, v[32:33], off
	global_load_dword v29, v[34:35], off
	global_load_dword v30, v[36:37], off
	global_load_dword v31, v[38:39], off
	v_add_u32_e32 v32, 0x4000, v56
	v_add_u32_e32 v34, 0x4100, v56
	v_add_u32_e32 v36, 0x4200, v56
	v_add_u32_e32 v38, 0x4300, v56
	v_add_u32_e32 v40, 0x4800, v56
	v_add_u32_e32 v42, 0x4900, v56
	v_add_u32_e32 v44, 0x4a00, v56
	v_add_u32_e32 v46, 0x4b00, v56
	v_ashrrev_i32_e32 v33, 31, v32
	v_ashrrev_i32_e32 v35, 31, v34
	v_ashrrev_i32_e32 v37, 31, v36
	v_ashrrev_i32_e32 v39, 31, v38
; template <bool PASS2, int DIRT>
; DI void mlstm_item(const Params& P, LAS unsigned char* lds, int st, int g) {
;     ...
;         for (int dkt = 0; dkt < 4; ++dkt)
; #pragma unroll
;             for (int e = 0; e < 16; ++e) C[dkt][e] = ec[(32 * dkt + (e & 3) + 8 * (e >> 2) + 4 * hh) * 256 + 32 * wid + r];
;         if (tid < 128) sN0[tid] = ((const float*)(P.ws + WS_ENTN))[((size_t)st * 16 + g) * 128 + tid];
	v_ashrrev_i32_e32 v41, 31, v40
	v_ashrrev_i32_e32 v43, 31, v42
	v_ashrrev_i32_e32 v45, 31, v44
	v_ashrrev_i32_e32 v47, 31, v46
	v_lshl_add_u64 v[32:33], v[32:33], 2, s[8:9]
	v_lshl_add_u64 v[34:35], v[34:35], 2, s[8:9]
	v_lshl_add_u64 v[36:37], v[36:37], 2, s[8:9]
	v_lshl_add_u64 v[38:39], v[38:39], 2, s[8:9]
	v_lshl_add_u64 v[40:41], v[40:41], 2, s[8:9]
	v_lshl_add_u64 v[42:43], v[42:43], 2, s[8:9]
	v_lshl_add_u64 v[44:45], v[44:45], 2, s[8:9]
	v_lshl_add_u64 v[46:47], v[46:47], 2, s[8:9]
	global_load_dword v32, v[32:33], off
	s_nop 0
	global_load_dword v33, v[34:35], off
	s_nop 0
	global_load_dword v34, v[36:37], off
	global_load_dword v35, v[38:39], off
	s_nop 0
	global_load_dword v36, v[40:41], off
	global_load_dword v37, v[42:43], off
	global_load_dword v38, v[44:45], off
	global_load_dword v39, v[46:47], off
	v_add_u32_e32 v40, 0x5000, v56
	v_add_u32_e32 v42, 0x5100, v56
	v_add_u32_e32 v44, 0x5200, v56
	v_add_u32_e32 v46, 0x5300, v56
	v_add_u32_e32 v48, 0x5800, v56
	v_add_u32_e32 v50, 0x5900, v56
	v_add_u32_e32 v52, 0x5a00, v56
	v_add_u32_e32 v54, 0x5b00, v56
	v_ashrrev_i32_e32 v41, 31, v40
	v_ashrrev_i32_e32 v43, 31, v42
	v_ashrrev_i32_e32 v45, 31, v44
	v_ashrrev_i32_e32 v47, 31, v46
	v_ashrrev_i32_e32 v49, 31, v48
	v_ashrrev_i32_e32 v51, 31, v50
	v_ashrrev_i32_e32 v53, 31, v52
	v_ashrrev_i32_e32 v55, 31, v54
	v_lshl_add_u64 v[40:41], v[40:41], 2, s[8:9]
	v_lshl_add_u64 v[42:43], v[42:43], 2, s[8:9]
	v_lshl_add_u64 v[44:45], v[44:45], 2, s[8:9]
	v_lshl_add_u64 v[46:47], v[46:47], 2, s[8:9]
	v_lshl_add_u64 v[48:49], v[48:49], 2, s[8:9]
	v_lshl_add_u64 v[50:51], v[50:51], 2, s[8:9]
	v_lshl_add_u64 v[52:53], v[52:53], 2, s[8:9]
	v_lshl_add_u64 v[54:55], v[54:55], 2, s[8:9]
	global_load_dword v40, v[40:41], off
	s_nop 0
	global_load_dword v41, v[42:43], off
	s_nop 0
	global_load_dword v42, v[44:45], off
	global_load_dword v43, v[46:47], off
	s_nop 0
	global_load_dword v44, v[48:49], off
	global_load_dword v45, v[50:51], off
	global_load_dword v46, v[52:53], off
	global_load_dword v47, v[54:55], off
	v_add_u32_e32 v48, 0x6000, v56
	v_add_u32_e32 v50, 0x6100, v56
	v_add_u32_e32 v52, 0x6200, v56
	v_add_u32_e32 v54, 0x6300, v56
	v_add_u32_e32 v58, 0x6800, v56
	v_add_u32_e32 v60, 0x6900, v56
	v_add_u32_e32 v62, 0x6a00, v56
	v_ashrrev_i32_e32 v49, 31, v48
	v_ashrrev_i32_e32 v51, 31, v50
	v_ashrrev_i32_e32 v53, 31, v52
	v_ashrrev_i32_e32 v55, 31, v54
	v_ashrrev_i32_e32 v59, 31, v58
	v_ashrrev_i32_e32 v61, 31, v60
	v_ashrrev_i32_e32 v63, 31, v62
	v_add_u32_e32 v64, 0x6b00, v56
	v_lshl_add_u64 v[48:49], v[48:49], 2, s[8:9]
	v_lshl_add_u64 v[50:51], v[50:51], 2, s[8:9]
	v_lshl_add_u64 v[52:53], v[52:53], 2, s[8:9]
	v_lshl_add_u64 v[54:55], v[54:55], 2, s[8:9]
	v_lshl_add_u64 v[58:59], v[58:59], 2, s[8:9]
	v_lshl_add_u64 v[60:61], v[60:61], 2, s[8:9]
	v_lshl_add_u64 v[62:63], v[62:63], 2, s[8:9]
	v_ashrrev_i32_e32 v65, 31, v64
	v_lshl_add_u64 v[64:65], v[64:65], 2, s[8:9]
	global_load_dword v48, v[48:49], off
	s_nop 0
	global_load_dword v49, v[50:51], off
	s_nop 0
	global_load_dword v50, v[52:53], off
	global_load_dword v51, v[54:55], off
	s_nop 0
	global_load_dword v52, v[58:59], off
	global_load_dword v53, v[60:61], off
	global_load_dword v54, v[62:63], off
	global_load_dword v55, v[64:65], off
	v_add_u32_e32 v58, 0x7000, v56
	v_add_u32_e32 v60, 0x7100, v56
	v_add_u32_e32 v62, 0x7200, v56
	v_ashrrev_i32_e32 v59, 31, v58
	v_ashrrev_i32_e32 v61, 31, v60
	v_ashrrev_i32_e32 v63, 31, v62
	v_add_u32_e32 v64, 0x7300, v56
	v_add_u32_e32 v66, 0x7800, v56
	v_add_u32_e32 v68, 0x7900, v56
	v_add_u32_e32 v72, 0x7a00, v56
	v_add_u32_e32 v56, 0x7b00, v56
	v_lshl_add_u64 v[58:59], v[58:59], 2, s[8:9]
	v_lshl_add_u64 v[60:61], v[60:61], 2, s[8:9]
	v_lshl_add_u64 v[62:63], v[62:63], 2, s[8:9]
	v_ashrrev_i32_e32 v65, 31, v64
	v_ashrrev_i32_e32 v67, 31, v66
	v_ashrrev_i32_e32 v69, 31, v68
	v_ashrrev_i32_e32 v73, 31, v72
	v_ashrrev_i32_e32 v57, 31, v56
	v_lshl_add_u64 v[64:65], v[64:65], 2, s[8:9]
	v_lshl_add_u64 v[66:67], v[66:67], 2, s[8:9]
	v_lshl_add_u64 v[68:69], v[68:69], 2, s[8:9]
	v_lshl_add_u64 v[72:73], v[72:73], 2, s[8:9]
	v_lshl_add_u64 v[74:75], v[56:57], 2, s[8:9]
	global_load_dword v56, v[58:59], off
	global_load_dword v57, v[60:61], off
	s_nop 0
	global_load_dword v58, v[62:63], off
	global_load_dword v59, v[64:65], off
	global_load_dword v60, v[66:67], off
	global_load_dword v61, v[68:69], off
	s_nop 0
	global_load_dword v62, v[72:73], off
	global_load_dword v63, v[74:75], off
	v_or_b32_e32 v64, s97, v70
	v_cmp_gt_i32_e32 vcc, s63, v64
	s_and_saveexec_b64 s[2:3], vcc
	s_cbranch_execz .LBB0_712
	s_lshl_b64 s[6:7], s[6:7], 9
	s_add_u32 s6, s55, s6
	s_addc_u32 s7, s56, s7
	v_ashrrev_i32_e32 v65, 31, v64
	v_lshl_add_u64 v[66:67], v[64:65], 2, s[6:7]
	global_load_dword v249, v[66:67], off
	v_lshl_add_u32 v250, v64, 2, 0
	v_add_u32_e32 v250, 0x1a600, v250
; #define LAS __attribute__((address_space(3)))
; DI float softcap(float x) { return 15.0f * tanhf(x * (1.0f / 15.0f)); }
; DI float logsigmoid(float y) { return fminf(y, 0.f) - log1pf(__expf(-fabsf(y))); }
; template <bool PASS2, int DIRT>
; DI void mlstm_item(const Params& P, LAS unsigned char* lds, int st, int g) {
;     ...
;         if (tid < 128) sN0[tid] = ((const float*)(P.ws + WS_ENTN))[((size_t)st * 16 + g) * 128 + tid];
;         if (tid == 0) sMISC[1] = ((const float*)(P.ws + WS_ENTN + 512 * 1024))[st * 16 + g];
;     } else {
;         if (tid < 128) sN0[tid] = 0.f;
;         if (tid == 0) sMISC[1] = -1e30f;
;     }
;     LAS float* sALL = SC + 10496 / 4;
;     LAS float* sCH = sALL + 8 * 3 * 128;
;     auto chunk_tok0 = [&](int ci) -> int { if (ctx_item) return T + b * CTXL + (dir ? (1 - ci) : ci) * 128;
;         const int cp = seg * 8 + ci; const int chunk = dir ? (NCHUNK - 1 - cp) : cp; return b * SEQ + chunk * 128; };
;     if (wid < nchunks) { const int t0c = chunk_tok0(wid);
;         const int p0 = dir ? 127 - 2 * lane : 2 * lane, p1 = dir ? 126 - 2 * lane : 2 * lane + 1;
;         const float* g0 = gates + (size_t)(t0c + p0) * 16; const float* g1 = gates + (size_t)(t0c + p1) * 16;
;         const float li0 = softcap(g0[dir * 8 + h]), li1 = softcap(g1[dir * 8 + h]); const float lf0 = logsigmoid(softcap(g0[dir * 8 + 4 + h])), lf1 = logsigmoid(softcap(g1[dir * 8 + 4 + h]));
.LBB0_712:
	s_or_b64 exec, exec, s[2:3]
	v_cmp_eq_u32_e32 vcc, 0, v64
	s_and_saveexec_b64 s[2:3], vcc
	s_cbranch_execz .LBB0_714
	s_ashr_i32 s43, s42, 31
	s_lshl_b64 s[6:7], s[42:43], 2
	s_add_u32 s6, s57, s6
	s_addc_u32 s7, s58, s7
	global_load_dword v251, v193, s[6:7]
	v_mov_b32_e32 v252, s65
.LBB0_714:
	s_or_b64 exec, exec, s[2:3]
	s_bfe_u32 s0, s4, 0x10002
	s_and_b32 s48, s4, 3
	s_cmp_gt_i32 s1, 7
	s_cbranch_scc1 .LBB0_734
	s_lshl_b32 s2, s0, 14
	s_lshl_b32 s3, s96, 10
	s_lshl_b32 s4, s1, 7
	v_and_b32_e32 v65, 63, v70
	s_or_b32 s2, s2, 0x3f80
	s_add_i32 s3, s3, s4
	s_sub_i32 s6, s2, s3
	v_lshlrev_b32_e32 v71, 1, v65
	v_bitop3_b32 v66, v71, s6, v200 bitop3:0xde
	v_ashrrev_i32_e32 v67, 31, v66
	v_lshlrev_b64 v[66:67], 6, v[66:67]
	v_lshl_add_u64 v[66:67], s[38:39], 0, v[66:67]
	s_lshl_b32 s40, s48, 2
	v_lshl_add_u64 v[66:67], v[66:67], 0, s[40:41]
	v_sub_u32_e32 v246, s6, v71
	v_add_u32_e32 v246, 0x7e, v246
	v_ashrrev_i32_e32 v247, 31, v246
	v_lshlrev_b64 v[246:247], 6, v[246:247]
	v_lshl_add_u64 v[246:247], s[38:39], 0, v[246:247]
	v_lshl_add_u64 v[246:247], v[246:247], 0, s[40:41]
	global_load_dword v68, v[66:67], off offset:32
	global_load_dword v244, v[66:67], off offset:48
	global_load_dword v248, v[246:247], off offset:32
	global_load_dword v245, v[246:247], off offset:48
	s_waitcnt vmcnt(0)
	v_cmp_gt_i32_e32 vcc, s63, v64
	s_and_saveexec_b64 s[2:3], vcc
	ds_write_b32 v250, v249
	s_or_b64 exec, exec, s[2:3]
	v_cmp_eq_u32_e32 vcc, 0, v64
	s_and_saveexec_b64 s[2:3], vcc
	ds_write_b32 v252, v251
	s_or_b64 exec, exec, s[2:3]
	v_mul_f32_e32 v72, 0x3d888889, v68
	v_cmp_nlt_f32_e64 s[2:3], |v72|, s66
	s_and_saveexec_b64 s[4:5], s[2:3]
	s_xor_b64 s[2:3], exec, s[4:5]
	s_cbranch_execz .LBB0_717
	v_add_f32_e64 v68, |v72|, |v72|
	v_mul_f32_e32 v69, 0x3fb8aa3b, v68
	v_rndne_f32_e32 v73, v69
	s_mov_b32 s4, 0x3fb8aa3b
	v_sub_f32_e32 v74, v69, v73
	v_fma_f32 v69, v68, s4, -v69
	v_fmac_f32_e32 v69, 0x32a5705f, v68
	v_add_f32_e32 v69, v74, v69
	v_cvt_i32_f32_e32 v73, v73
	v_exp_f32_e32 v69, v69
	v_cmp_ngt_f32_e64 s[4:5], s68, v68
	v_ldexp_f32 v69, v69, v73
	s_nop 0
	v_cndmask_b32_e64 v69, 0, v69, s[4:5]
	v_cmp_nlt_f32_e64 s[4:5], s69, v68
	s_nop 1
	v_cndmask_b32_e64 v68, v201, v69, s[4:5]
	v_add_f32_e32 v68, 1.0, v68
	v_rcp_f32_e32 v68, v68
	s_nop 0
	v_fma_f32 v73, v68, -2.0, 1.0

; template <bool PASS2, int DIRT>
; DI void mlstm_item(const Params& P, LAS unsigned char* lds, int st, int g) {
;     ...
;     __syncthreads();
;     if (PASS2) {
;         const float* ec = (const float*)(P.ws + WS_ENTC) + ((size_t)st * 16 + g) * 32768;
; #pragma unroll
;         for (int dkt = 0; dkt < 4; ++dkt)
; #pragma unroll
;             for (int e = 0; e < 16; ++e) C[dkt][e] = ec[(32 * dkt + (e & 3) + 8 * (e >> 2) + 4 * hh) * 256 + 32 * wid + r];
.LBB0_766:
	s_and_b64 vcc, exec, s[2:3]
	s_cbranch_vccz .LBB0_708
	s_waitcnt lgkmcnt(0)
	v_readfirstlane_b32 s0, v195
	s_mov_b32 s43, s41
	s_lshl_b32 s97, s0, 6
	s_lshl_b64 s[2:3], s[42:43], 17
	s_add_u32 s4, s53, s2
	s_waitcnt vmcnt(2)
	v_mbcnt_lo_u32_b32 v70, -1, 0
	v_mbcnt_hi_u32_b32 v70, -1, v70
	s_addc_u32 s5, s54, s3
	v_lshlrev_b32_e32 v0, 5, v70
	s_lshl_b32 s44, s0, 5
	v_and_b32_e32 v0, 0x400, v0
	v_and_or_b32 v1, v70, 31, s44
	v_add_u32_e32 v56, v0, v1
	v_add_u32_e32 v0, 0x800, v56
	v_ashrrev_i32_e32 v1, 31, v0
	v_lshl_add_u64 v[6:7], v[0:1], 2, s[4:5]
	v_add_u32_e32 v0, 0x900, v56
	v_ashrrev_i32_e32 v1, 31, v0
	v_lshl_add_u64 v[8:9], v[0:1], 2, s[4:5]
	v_add_u32_e32 v0, 0xa00, v56
	v_ashrrev_i32_e32 v1, 31, v0
	v_lshl_add_u64 v[10:11], v[0:1], 2, s[4:5]
	v_add_u32_e32 v0, 0xb00, v56
	v_ashrrev_i32_e32 v57, 31, v56
	v_ashrrev_i32_e32 v1, 31, v0
	v_lshl_add_u64 v[4:5], v[56:57], 2, s[4:5]
	v_lshl_add_u64 v[12:13], v[0:1], 2, s[4:5]
	s_waitcnt vmcnt(0)
	s_barrier
	global_load_dword v0, v[4:5], off
	global_load_dword v1, v[4:5], off offset:1024
	global_load_dword v2, v[4:5], off offset:2048
	global_load_dword v3, v[4:5], off offset:3072
	s_nop 0
	global_load_dword v4, v[6:7], off
	global_load_dword v5, v[8:9], off
	s_nop 0
	global_load_dword v6, v[10:11], off
	global_load_dword v7, v[12:13], off
	v_add_u32_e32 v8, 0x1000, v56
	v_add_u32_e32 v10, 0x1100, v56
	v_add_u32_e32 v12, 0x1200, v56
	v_add_u32_e32 v14, 0x1300, v56
	v_add_u32_e32 v16, 0x1800, v56
	v_add_u32_e32 v18, 0x1900, v56
	v_add_u32_e32 v20, 0x1a00, v56
	v_add_u32_e32 v22, 0x1b00, v56
	v_ashrrev_i32_e32 v9, 31, v8
	v_ashrrev_i32_e32 v11, 31, v10
	v_ashrrev_i32_e32 v13, 31, v12
	v_ashrrev_i32_e32 v15, 31, v14
	v_ashrrev_i32_e32 v17, 31, v16
	v_ashrrev_i32_e32 v19, 31, v18
	v_ashrrev_i32_e32 v21, 31, v20
	v_ashrrev_i32_e32 v23, 31, v22
	v_lshl_add_u64 v[8:9], v[8:9], 2, s[4:5]
	v_lshl_add_u64 v[10:11], v[10:11], 2, s[4:5]
	v_lshl_add_u64 v[12:13], v[12:13], 2, s[4:5]
	v_lshl_add_u64 v[14:15], v[14:15], 2, s[4:5]
	v_lshl_add_u64 v[16:17], v[16:17], 2, s[4:5]
	v_lshl_add_u64 v[18:19], v[18:19], 2, s[4:5]
	v_lshl_add_u64 v[20:21], v[20:21], 2, s[4:5]
	v_lshl_add_u64 v[22:23], v[22:23], 2, s[4:5]
	global_load_dword v8, v[8:9], off
	s_nop 0
	global_load_dword v9, v[10:11], off
	s_nop 0
	global_load_dword v10, v[12:13], off
	global_load_dword v11, v[14:15], off
	s_nop 0
	global_load_dword v12, v[16:17], off
	global_load_dword v13, v[18:19], off
	global_load_dword v14, v[20:21], off
	global_load_dword v15, v[22:23], off
	v_add_u32_e32 v16, 0x2000, v56
	v_add_u32_e32 v18, 0x2100, v56
	v_add_u32_e32 v20, 0x2200, v56
	v_add_u32_e32 v22, 0x2300, v56
	v_add_u32_e32 v24, 0x2800, v56
	v_add_u32_e32 v26, 0x2900, v56
	v_add_u32_e32 v28, 0x2a00, v56
	v_add_u32_e32 v30, 0x2b00, v56
	v_ashrrev_i32_e32 v17, 31, v16
	v_ashrrev_i32_e32 v19, 31, v18
	v_ashrrev_i32_e32 v21, 31, v20
	v_ashrrev_i32_e32 v23, 31, v22
	v_ashrrev_i32_e32 v25, 31, v24
	v_ashrrev_i32_e32 v27, 31, v26
	v_ashrrev_i32_e32 v29, 31, v28
	v_ashrrev_i32_e32 v31, 31, v30
	v_lshl_add_u64 v[16:17], v[16:17], 2, s[4:5]
	v_lshl_add_u64 v[18:19], v[18:19], 2, s[4:5]
	v_lshl_add_u64 v[20:21], v[20:21], 2, s[4:5]
	v_lshl_add_u64 v[22:23], v[22:23], 2, s[4:5]
	v_lshl_add_u64 v[24:25], v[24:25], 2, s[4:5]
	v_lshl_add_u64 v[26:27], v[26:27], 2, s[4:5]
	v_lshl_add_u64 v[28:29], v[28:29], 2, s[4:5]
	v_lshl_add_u64 v[30:31], v[30:31], 2, s[4:5]
	global_load_dword v16, v[16:17], off
	s_nop 0
	global_load_dword v17, v[18:19], off
	s_nop 0
	global_load_dword v18, v[20:21], off
	global_load_dword v19, v[22:23], off
	s_nop 0
	global_load_dword v20, v[24:25], off
	global_load_dword v21, v[26:27], off
	global_load_dword v22, v[28:29], off
	global_load_dword v23, v[30:31], off
	v_add_u32_e32 v24, 0x3000, v56
	v_add_u32_e32 v26, 0x3100, v56
	v_add_u32_e32 v28, 0x3200, v56
	v_add_u32_e32 v30, 0x3300, v56
	v_add_u32_e32 v32, 0x3800, v56
	v_add_u32_e32 v34, 0x3900, v56
	v_add_u32_e32 v36, 0x3a00, v56
	v_add_u32_e32 v38, 0x3b00, v56
	v_ashrrev_i32_e32 v25, 31, v24
	v_ashrrev_i32_e32 v27, 31, v26
	v_ashrrev_i32_e32 v29, 31, v28
	v_ashrrev_i32_e32 v31, 31, v30
	v_ashrrev_i32_e32 v33, 31, v32
	v_ashrrev_i32_e32 v35, 31, v34
	v_ashrrev_i32_e32 v37, 31, v36
	v_ashrrev_i32_e32 v39, 31, v38
	v_lshl_add_u64 v[24:25], v[24:25], 2, s[4:5]
	v_lshl_add_u64 v[26:27], v[26:27], 2, s[4:5]
	v_lshl_add_u64 v[28:29], v[28:29], 2, s[4:5]
	v_lshl_add_u64 v[30:31], v[30:31], 2, s[4:5]
	v_lshl_add_u64 v[32:33], v[32:33], 2, s[4:5]
	v_lshl_add_u64 v[34:35], v[34:35], 2, s[4:5]
	v_lshl_add_u64 v[36:37], v[36:37], 2, s[4:5]
	v_lshl_add_u64 v[38:39], v[38:39], 2, s[4:5]
	global_load_dword v24, v[24:25], off
	s_nop 0
	global_load_dword v25, v[26:27], off
	s_nop 0
	global_load_dword v26, v[28:29], off
	global_load_dword v27, v[30:31], off
	s_nop 0
	global_load_dword v28, v[32:33], off
	global_load_dword v29, v[34:35], off
	global_load_dword v30, v[36:37], off
	global_load_dword v31, v[38:39], off
	v_add_u32_e32 v32, 0x4000, v56
	v_add_u32_e32 v34, 0x4100, v56
	v_add_u32_e32 v36, 0x4200, v56
	v_add_u32_e32 v38, 0x4300, v56
	v_add_u32_e32 v40, 0x4800, v56
	v_add_u32_e32 v42, 0x4900, v56
	v_add_u32_e32 v44, 0x4a00, v56
	v_add_u32_e32 v46, 0x4b00, v56
	v_ashrrev_i32_e32 v33, 31, v32
	v_ashrrev_i32_e32 v35, 31, v34
	v_ashrrev_i32_e32 v37, 31, v36
	v_ashrrev_i32_e32 v39, 31, v38
	v_ashrrev_i32_e32 v41, 31, v40
	v_ashrrev_i32_e32 v43, 31, v42
	v_ashrrev_i32_e32 v45, 31, v44
	v_ashrrev_i32_e32 v47, 31, v46
	v_lshl_add_u64 v[32:33], v[32:33], 2, s[4:5]
	v_lshl_add_u64 v[34:35], v[34:35], 2, s[4:5]
	v_lshl_add_u64 v[36:37], v[36:37], 2, s[4:5]
	v_lshl_add_u64 v[38:39], v[38:39], 2, s[4:5]
; #define LAS __attribute__((address_space(3)))
; DI float softcap(float x) { return 15.0f * tanhf(x * (1.0f / 15.0f)); }
; DI float logsigmoid(float y) { return fminf(y, 0.f) - log1pf(__expf(-fabsf(y))); }
; template <bool PASS2, int DIRT>
; DI void mlstm_item(const Params& P, LAS unsigned char* lds, int st, int g) {
;     ...
;         for (int dkt = 0; dkt < 4; ++dkt)
; #pragma unroll
;             for (int e = 0; e < 16; ++e) C[dkt][e] = ec[(32 * dkt + (e & 3) + 8 * (e >> 2) + 4 * hh) * 256 + 32 * wid + r];
;         if (tid < 128) sN0[tid] = ((const float*)(P.ws + WS_ENTN))[((size_t)st * 16 + g) * 128 + tid];
;         if (tid == 0) sMISC[1] = ((const float*)(P.ws + WS_ENTN + 512 * 1024))[st * 16 + g];
;     } else {
;         if (tid < 128) sN0[tid] = 0.f;
;         if (tid == 0) sMISC[1] = -1e30f;
;     }
;     LAS float* sALL = SC + 10496 / 4;
;     LAS float* sCH = sALL + 8 * 3 * 128;
;     auto chunk_tok0 = [&](int ci) -> int { if (ctx_item) return T + b * CTXL + (dir ? (1 - ci) : ci) * 128;
;         const int cp = seg * 8 + ci; const int chunk = dir ? (NCHUNK - 1 - cp) : cp; return b * SEQ + chunk * 128; };
;     if (wid < nchunks) { const int t0c = chunk_tok0(wid);
;         const int p0 = dir ? 127 - 2 * lane : 2 * lane, p1 = dir ? 126 - 2 * lane : 2 * lane + 1;
;         const float* g0 = gates + (size_t)(t0c + p0) * 16; const float* g1 = gates + (size_t)(t0c + p1) * 16;
;         const float li0 = softcap(g0[dir * 8 + h]), li1 = softcap(g1[dir * 8 + h]); const float lf0 = logsigmoid(softcap(g0[dir * 8 + 4 + h])), lf1 = logsigmoid(softcap(g1[dir * 8 + 4 + h]));
	v_lshl_add_u64 v[40:41], v[40:41], 2, s[4:5]
	v_lshl_add_u64 v[42:43], v[42:43], 2, s[4:5]
	v_lshl_add_u64 v[44:45], v[44:45], 2, s[4:5]
	v_lshl_add_u64 v[46:47], v[46:47], 2, s[4:5]
	global_load_dword v32, v[32:33], off
	s_nop 0
	global_load_dword v33, v[34:35], off
	s_nop 0
	global_load_dword v34, v[36:37], off
	global_load_dword v35, v[38:39], off
	s_nop 0
	global_load_dword v36, v[40:41], off
	global_load_dword v37, v[42:43], off
	global_load_dword v38, v[44:45], off
	global_load_dword v39, v[46:47], off
	v_add_u32_e32 v40, 0x5000, v56
	v_add_u32_e32 v42, 0x5100, v56
	v_add_u32_e32 v44, 0x5200, v56
	v_add_u32_e32 v46, 0x5300, v56
	v_add_u32_e32 v48, 0x5800, v56
	v_add_u32_e32 v50, 0x5900, v56
	v_add_u32_e32 v52, 0x5a00, v56
	v_add_u32_e32 v54, 0x5b00, v56
	v_ashrrev_i32_e32 v41, 31, v40
	v_ashrrev_i32_e32 v43, 31, v42
	v_ashrrev_i32_e32 v45, 31, v44
	v_ashrrev_i32_e32 v47, 31, v46
	v_ashrrev_i32_e32 v49, 31, v48
	v_ashrrev_i32_e32 v51, 31, v50
	v_ashrrev_i32_e32 v53, 31, v52
	v_ashrrev_i32_e32 v55, 31, v54
	v_lshl_add_u64 v[40:41], v[40:41], 2, s[4:5]
	v_lshl_add_u64 v[42:43], v[42:43], 2, s[4:5]
	v_lshl_add_u64 v[44:45], v[44:45], 2, s[4:5]
	v_lshl_add_u64 v[46:47], v[46:47], 2, s[4:5]
	v_lshl_add_u64 v[48:49], v[48:49], 2, s[4:5]
	v_lshl_add_u64 v[50:51], v[50:51], 2, s[4:5]
	v_lshl_add_u64 v[52:53], v[52:53], 2, s[4:5]
	v_lshl_add_u64 v[54:55], v[54:55], 2, s[4:5]
	global_load_dword v40, v[40:41], off
	s_nop 0
	global_load_dword v41, v[42:43], off
	s_nop 0
	global_load_dword v42, v[44:45], off
	global_load_dword v43, v[46:47], off
	s_nop 0
	global_load_dword v44, v[48:49], off
	global_load_dword v45, v[50:51], off
	global_load_dword v46, v[52:53], off
	global_load_dword v47, v[54:55], off
	v_add_u32_e32 v48, 0x6000, v56
	v_add_u32_e32 v50, 0x6100, v56
	v_add_u32_e32 v52, 0x6200, v56
	v_add_u32_e32 v54, 0x6300, v56
	v_add_u32_e32 v58, 0x6800, v56
	v_add_u32_e32 v60, 0x6900, v56
	v_add_u32_e32 v62, 0x6a00, v56
	v_ashrrev_i32_e32 v49, 31, v48
	v_ashrrev_i32_e32 v51, 31, v50
	v_ashrrev_i32_e32 v53, 31, v52
	v_ashrrev_i32_e32 v55, 31, v54
	v_ashrrev_i32_e32 v59, 31, v58
	v_ashrrev_i32_e32 v61, 31, v60
	v_ashrrev_i32_e32 v63, 31, v62
	v_add_u32_e32 v64, 0x6b00, v56
	v_lshl_add_u64 v[48:49], v[48:49], 2, s[4:5]
	v_lshl_add_u64 v[50:51], v[50:51], 2, s[4:5]
	v_lshl_add_u64 v[52:53], v[52:53], 2, s[4:5]
	v_lshl_add_u64 v[54:55], v[54:55], 2, s[4:5]
	v_lshl_add_u64 v[58:59], v[58:59], 2, s[4:5]
	v_lshl_add_u64 v[60:61], v[60:61], 2, s[4:5]
	v_lshl_add_u64 v[62:63], v[62:63], 2, s[4:5]
	v_ashrrev_i32_e32 v65, 31, v64
	v_lshl_add_u64 v[64:65], v[64:65], 2, s[4:5]
	global_load_dword v48, v[48:49], off
	s_nop 0
	global_load_dword v49, v[50:51], off
	s_nop 0
	global_load_dword v50, v[52:53], off
	global_load_dword v51, v[54:55], off
	s_nop 0
	global_load_dword v52, v[58:59], off
	global_load_dword v53, v[60:61], off
	global_load_dword v54, v[62:63], off
	global_load_dword v55, v[64:65], off
	v_add_u32_e32 v58, 0x7000, v56
	v_add_u32_e32 v60, 0x7100, v56
	v_add_u32_e32 v62, 0x7200, v56
	v_ashrrev_i32_e32 v59, 31, v58
	v_ashrrev_i32_e32 v61, 31, v60
	v_ashrrev_i32_e32 v63, 31, v62
	v_add_u32_e32 v64, 0x7300, v56
	v_add_u32_e32 v66, 0x7800, v56
	v_add_u32_e32 v68, 0x7900, v56
	v_add_u32_e32 v72, 0x7a00, v56
	v_add_u32_e32 v56, 0x7b00, v56
	v_lshl_add_u64 v[58:59], v[58:59], 2, s[4:5]
	v_lshl_add_u64 v[60:61], v[60:61], 2, s[4:5]
	v_lshl_add_u64 v[62:63], v[62:63], 2, s[4:5]
	v_ashrrev_i32_e32 v65, 31, v64
	v_ashrrev_i32_e32 v67, 31, v66
	v_ashrrev_i32_e32 v69, 31, v68
	v_ashrrev_i32_e32 v73, 31, v72
	v_ashrrev_i32_e32 v57, 31, v56
	v_lshl_add_u64 v[64:65], v[64:65], 2, s[4:5]
	v_lshl_add_u64 v[66:67], v[66:67], 2, s[4:5]
	v_lshl_add_u64 v[68:69], v[68:69], 2, s[4:5]
	v_lshl_add_u64 v[72:73], v[72:73], 2, s[4:5]
	v_lshl_add_u64 v[74:75], v[56:57], 2, s[4:5]
	global_load_dword v56, v[58:59], off
	global_load_dword v57, v[60:61], off
	s_nop 0
	global_load_dword v58, v[62:63], off
	global_load_dword v59, v[64:65], off
	global_load_dword v60, v[66:67], off
	global_load_dword v61, v[68:69], off
	s_nop 0
	global_load_dword v62, v[72:73], off
	global_load_dword v63, v[74:75], off
	v_or_b32_e32 v64, s97, v70
	v_cmp_gt_i32_e32 vcc, s63, v64
	s_and_saveexec_b64 s[2:3], vcc
	s_cbranch_execz .LBB0_769
	s_lshl_b64 s[4:5], s[42:43], 9
	s_add_u32 s4, s55, s4
	s_addc_u32 s5, s56, s5
	v_ashrrev_i32_e32 v65, 31, v64
	v_lshl_add_u64 v[66:67], v[64:65], 2, s[4:5]
	global_load_dword v249, v[66:67], off
	v_lshl_add_u32 v250, v64, 2, 0
	v_add_u32_e32 v250, 0x1a600, v250
.LBB0_769:
	s_or_b64 exec, exec, s[2:3]
	v_cmp_eq_u32_e32 vcc, 0, v64
	s_and_saveexec_b64 s[2:3], vcc
	s_cbranch_execz .LBB0_771
	s_lshl_b64 s[4:5], s[42:43], 2
	s_add_u32 s4, s57, s4
	s_addc_u32 s5, s58, s5
	global_load_dword v251, v193, s[4:5]
	v_mov_b32_e32 v252, s65
.LBB0_771:
	s_or_b64 exec, exec, s[2:3]
	s_lshr_b32 s1, s42, 6
	s_bfe_u32 s48, s42, 0x20004
	s_cmp_gt_i32 s0, 7
	s_cbranch_scc1 .LBB0_791
	s_lshl_b32 s2, s1, 14
	s_lshl_b32 s3, s96, 10
	v_and_b32_e32 v65, 63, v70
	s_lshl_b32 s4, s0, 7
	s_or_b32 s2, s2, s3
	s_add_i32 s2, s2, s4
	v_lshlrev_b32_e32 v71, 1, v65
	v_or_b32_e32 v68, s2, v71
	v_ashrrev_i32_e32 v69, 31, v68
	v_lshlrev_b64 v[66:67], 6, v[68:69]
	v_lshl_add_u64 v[66:67], s[38:39], 0, v[66:67]
	s_lshl_b32 s40, s48, 2
	v_lshl_add_u64 v[72:73], v[66:67], 0, s[40:41]
	v_or_b32_e32 v246, 1, v68
	v_ashrrev_i32_e32 v247, 31, v246
	v_lshlrev_b64 v[246:247], 6, v[246:247]
	v_lshl_add_u64 v[246:247], s[38:39], 0, v[246:247]
	v_lshl_add_u64 v[246:247], v[246:247], 0, s[40:41]
	global_load_dword v69, v[72:73], off
	global_load_dword v244, v[72:73], off offset:16
	global_load_dword v248, v[246:247], off
	global_load_dword v245, v[246:247], off offset:16
	s_waitcnt vmcnt(0)
	v_cmp_gt_i32_e32 vcc, s63, v64
	s_and_saveexec_b64 s[2:3], vcc
	ds_write_b32 v250, v249
	s_or_b64 exec, exec, s[2:3]
	v_cmp_eq_u32_e32 vcc, 0, v64
	s_and_saveexec_b64 s[2:3], vcc
	ds_write_b32 v252, v251
	s_or_b64 exec, exec, s[2:3]
	v_mul_f32_e32 v72, 0x3d888889, v69
	v_cmp_nlt_f32_e64 s[2:3], |v72|, s66
	s_and_saveexec_b64 s[4:5], s[2:3]
	s_xor_b64 s[2:3], exec, s[4:5]
	s_cbranch_execz .LBB0_774
	v_add_f32_e64 v69, |v72|, |v72|
	v_mul_f32_e32 v73, 0x3fb8aa3b, v69
	v_rndne_f32_e32 v74, v73
	s_mov_b32 s4, 0x3fb8aa3b
	v_sub_f32_e32 v75, v73, v74
	v_fma_f32 v73, v69, s4, -v73
	v_fmac_f32_e32 v73, 0x32a5705f, v69
	v_add_f32_e32 v73, v75, v73
	v_cvt_i32_f32_e32 v74, v74
	v_exp_f32_e32 v73, v73
	v_cmp_ngt_f32_e64 s[4:5], s68, v69
	v_ldexp_f32 v73, v73, v74
	s_nop 0
	v_cndmask_b32_e64 v73, 0, v73, s[4:5]
	v_cmp_nlt_f32_e64 s[4:5], s69, v69
	s_nop 1
	v_cndmask_b32_e64 v69, v201, v73, s[4:5]
	v_add_f32_e32 v69, 1.0, v69
	v_rcp_f32_e32 v69, v69
	s_nop 0
	v_fma_f32 v73, v69, -2.0, 1.0
